# P9 wave sums on the register crossbar (DPP quad/mirror + v_permlane16/32_swap) instead of twelve ds_bpermute hops per row
# baseline (speedup 1.0000x reference)
.Lp9_nold_A:
	v_cvt_pk_f32_fp8_e32 v[234:235], v64
	v_cvt_pk_f32_fp8_sdwa v[236:237], v64 src0_sel:WORD_1
	v_cvt_pk_f32_fp8_e32 v[238:239], v65
	v_cvt_pk_f32_fp8_sdwa v[240:241], v65 src0_sel:WORD_1
	v_lshlrev_b32_e32 v242, 16, v96
	v_and_b32_e32 v243, 0xffff0000, v96
	v_pk_add_f32 v[234:235], v[234:235], v[238:239]
	v_pk_add_f32 v[236:237], v[236:237], v[240:241]
	v_cvt_pk_f32_fp8_e32 v[238:239], v66
	v_cvt_pk_f32_fp8_sdwa v[240:241], v66 src0_sel:WORD_1
	v_lshlrev_b32_e32 v244, 16, v97
	v_and_b32_e32 v245, 0xffff0000, v97
	v_pk_add_f32 v[234:235], v[234:235], v[238:239]
	v_pk_add_f32 v[236:237], v[236:237], v[240:241]
	v_cvt_pk_f32_fp8_e32 v[238:239], v67
	v_cvt_pk_f32_fp8_sdwa v[240:241], v67 src0_sel:WORD_1
	v_pk_mul_f32 v[242:243], v[242:243], s[8:9] op_sel_hi:[1,0]
	v_pk_mul_f32 v[244:245], v[244:245], s[8:9] op_sel_hi:[1,0]
	v_pk_add_f32 v[234:235], v[234:235], v[238:239]
	v_pk_add_f32 v[236:237], v[236:237], v[240:241]
	v_pk_fma_f32 v[112:113], v[112:113], v[234:235], v[242:243]
	v_pk_fma_f32 v[114:115], v[114:115], v[236:237], v[244:245]
	v_pk_add_f32 v[246:247], v[112:113], v[114:115]
	v_cvt_pk_f32_fp8_e32 v[234:235], v68
	v_cvt_pk_f32_fp8_sdwa v[236:237], v68 src0_sel:WORD_1
	v_cvt_pk_f32_fp8_e32 v[238:239], v69
	v_cvt_pk_f32_fp8_sdwa v[240:241], v69 src0_sel:WORD_1
	v_lshlrev_b32_e32 v242, 16, v98
	v_and_b32_e32 v243, 0xffff0000, v98
	v_pk_add_f32 v[234:235], v[234:235], v[238:239]
	v_pk_add_f32 v[236:237], v[236:237], v[240:241]
	v_cvt_pk_f32_fp8_e32 v[238:239], v70
	v_cvt_pk_f32_fp8_sdwa v[240:241], v70 src0_sel:WORD_1
	v_lshlrev_b32_e32 v244, 16, v99
	v_and_b32_e32 v245, 0xffff0000, v99
	v_pk_add_f32 v[234:235], v[234:235], v[238:239]
	v_pk_add_f32 v[236:237], v[236:237], v[240:241]
	v_cvt_pk_f32_fp8_e32 v[238:239], v71
	v_cvt_pk_f32_fp8_sdwa v[240:241], v71 src0_sel:WORD_1
	v_pk_mul_f32 v[242:243], v[242:243], s[8:9] op_sel_hi:[1,0]
	v_pk_mul_f32 v[244:245], v[244:245], s[8:9] op_sel_hi:[1,0]
	v_pk_add_f32 v[234:235], v[234:235], v[238:239]
	v_pk_add_f32 v[236:237], v[236:237], v[240:241]
	v_pk_fma_f32 v[116:117], v[116:117], v[234:235], v[242:243]
	v_pk_fma_f32 v[118:119], v[118:119], v[236:237], v[244:245]
	v_pk_add_f32 v[246:247], v[246:247], v[116:117]
	v_pk_add_f32 v[246:247], v[246:247], v[118:119]
	v_cvt_pk_f32_fp8_e32 v[234:235], v72
	v_cvt_pk_f32_fp8_sdwa v[236:237], v72 src0_sel:WORD_1
	v_cvt_pk_f32_fp8_e32 v[238:239], v73
	v_cvt_pk_f32_fp8_sdwa v[240:241], v73 src0_sel:WORD_1
	v_lshlrev_b32_e32 v242, 16, v100
	v_and_b32_e32 v243, 0xffff0000, v100
	v_pk_add_f32 v[234:235], v[234:235], v[238:239]
	v_pk_add_f32 v[236:237], v[236:237], v[240:241]
	v_cvt_pk_f32_fp8_e32 v[238:239], v74
	v_cvt_pk_f32_fp8_sdwa v[240:241], v74 src0_sel:WORD_1
	v_lshlrev_b32_e32 v244, 16, v101
	v_and_b32_e32 v245, 0xffff0000, v101
	v_pk_add_f32 v[234:235], v[234:235], v[238:239]
	v_pk_add_f32 v[236:237], v[236:237], v[240:241]
	v_cvt_pk_f32_fp8_e32 v[238:239], v75
	v_cvt_pk_f32_fp8_sdwa v[240:241], v75 src0_sel:WORD_1
	v_pk_mul_f32 v[242:243], v[242:243], s[8:9] op_sel_hi:[1,0]
	v_pk_mul_f32 v[244:245], v[244:245], s[8:9] op_sel_hi:[1,0]
	v_pk_add_f32 v[234:235], v[234:235], v[238:239]
	v_pk_add_f32 v[236:237], v[236:237], v[240:241]
	v_pk_fma_f32 v[120:121], v[120:121], v[234:235], v[242:243]
	v_pk_fma_f32 v[122:123], v[122:123], v[236:237], v[244:245]
	v_pk_add_f32 v[246:247], v[246:247], v[120:121]
	v_pk_add_f32 v[246:247], v[246:247], v[122:123]
	v_cvt_pk_f32_fp8_e32 v[234:235], v76
	v_cvt_pk_f32_fp8_sdwa v[236:237], v76 src0_sel:WORD_1
	v_cvt_pk_f32_fp8_e32 v[238:239], v77
	v_cvt_pk_f32_fp8_sdwa v[240:241], v77 src0_sel:WORD_1
	v_lshlrev_b32_e32 v242, 16, v102
	v_and_b32_e32 v243, 0xffff0000, v102
	v_pk_add_f32 v[234:235], v[234:235], v[238:239]
	v_pk_add_f32 v[236:237], v[236:237], v[240:241]
	v_cvt_pk_f32_fp8_e32 v[238:239], v78
	v_cvt_pk_f32_fp8_sdwa v[240:241], v78 src0_sel:WORD_1
	v_lshlrev_b32_e32 v244, 16, v103
	v_and_b32_e32 v245, 0xffff0000, v103
	v_pk_add_f32 v[234:235], v[234:235], v[238:239]
	v_pk_add_f32 v[236:237], v[236:237], v[240:241]
	v_cvt_pk_f32_fp8_e32 v[238:239], v79
	v_cvt_pk_f32_fp8_sdwa v[240:241], v79 src0_sel:WORD_1
	v_pk_mul_f32 v[242:243], v[242:243], s[8:9] op_sel_hi:[1,0]
	v_pk_mul_f32 v[244:245], v[244:245], s[8:9] op_sel_hi:[1,0]
	v_pk_add_f32 v[234:235], v[234:235], v[238:239]
	v_pk_add_f32 v[236:237], v[236:237], v[240:241]
	v_pk_fma_f32 v[124:125], v[124:125], v[234:235], v[242:243]
	v_pk_fma_f32 v[126:127], v[126:127], v[236:237], v[244:245]
	v_pk_add_f32 v[246:247], v[246:247], v[124:125]
	v_pk_add_f32 v[246:247], v[246:247], v[126:127]
	v_cvt_pk_f32_fp8_e32 v[234:235], v80
	v_cvt_pk_f32_fp8_sdwa v[236:237], v80 src0_sel:WORD_1
	v_cvt_pk_f32_fp8_e32 v[238:239], v81
	v_cvt_pk_f32_fp8_sdwa v[240:241], v81 src0_sel:WORD_1
	v_lshlrev_b32_e32 v242, 16, v104
	v_and_b32_e32 v243, 0xffff0000, v104
	v_pk_add_f32 v[234:235], v[234:235], v[238:239]
	v_pk_add_f32 v[236:237], v[236:237], v[240:241]
	v_cvt_pk_f32_fp8_e32 v[238:239], v82
	v_cvt_pk_f32_fp8_sdwa v[240:241], v82 src0_sel:WORD_1
	v_lshlrev_b32_e32 v244, 16, v105
	v_and_b32_e32 v245, 0xffff0000, v105
	v_pk_add_f32 v[234:235], v[234:235], v[238:239]
	v_pk_add_f32 v[236:237], v[236:237], v[240:241]
	v_cvt_pk_f32_fp8_e32 v[238:239], v83
	v_cvt_pk_f32_fp8_sdwa v[240:241], v83 src0_sel:WORD_1
	v_pk_mul_f32 v[242:243], v[242:243], s[8:9] op_sel_hi:[1,0]
	v_pk_mul_f32 v[244:245], v[244:245], s[8:9] op_sel_hi:[1,0]
	v_pk_add_f32 v[234:235], v[234:235], v[238:239]
	v_pk_add_f32 v[236:237], v[236:237], v[240:241]
	v_pk_fma_f32 v[128:129], v[128:129], v[234:235], v[242:243]
	v_pk_fma_f32 v[130:131], v[130:131], v[236:237], v[244:245]
	v_pk_add_f32 v[246:247], v[246:247], v[128:129]
	v_pk_add_f32 v[246:247], v[246:247], v[130:131]
	v_cvt_pk_f32_fp8_e32 v[234:235], v84
	v_cvt_pk_f32_fp8_sdwa v[236:237], v84 src0_sel:WORD_1
	v_cvt_pk_f32_fp8_e32 v[238:239], v85
	v_cvt_pk_f32_fp8_sdwa v[240:241], v85 src0_sel:WORD_1
	v_lshlrev_b32_e32 v242, 16, v106
	v_and_b32_e32 v243, 0xffff0000, v106
	v_pk_add_f32 v[234:235], v[234:235], v[238:239]
	v_pk_add_f32 v[236:237], v[236:237], v[240:241]
	v_cvt_pk_f32_fp8_e32 v[238:239], v86
	v_cvt_pk_f32_fp8_sdwa v[240:241], v86 src0_sel:WORD_1
	v_lshlrev_b32_e32 v244, 16, v107
	v_and_b32_e32 v245, 0xffff0000, v107
	v_pk_add_f32 v[234:235], v[234:235], v[238:239]
	v_pk_add_f32 v[236:237], v[236:237], v[240:241]
	v_cvt_pk_f32_fp8_e32 v[238:239], v87
	v_cvt_pk_f32_fp8_sdwa v[240:241], v87 src0_sel:WORD_1
	v_pk_mul_f32 v[242:243], v[242:243], s[8:9] op_sel_hi:[1,0]
	v_pk_mul_f32 v[244:245], v[244:245], s[8:9] op_sel_hi:[1,0]
	v_pk_add_f32 v[234:235], v[234:235], v[238:239]
	v_pk_add_f32 v[236:237], v[236:237], v[240:241]
	v_pk_fma_f32 v[132:133], v[132:133], v[234:235], v[242:243]
	v_pk_fma_f32 v[134:135], v[134:135], v[236:237], v[244:245]
	v_pk_add_f32 v[246:247], v[246:247], v[132:133]
	v_pk_add_f32 v[246:247], v[246:247], v[134:135]
	v_cvt_pk_f32_fp8_e32 v[234:235], v88
	v_cvt_pk_f32_fp8_sdwa v[236:237], v88 src0_sel:WORD_1
	v_cvt_pk_f32_fp8_e32 v[238:239], v89
	v_cvt_pk_f32_fp8_sdwa v[240:241], v89 src0_sel:WORD_1
	v_lshlrev_b32_e32 v242, 16, v108
	v_and_b32_e32 v243, 0xffff0000, v108
	v_pk_add_f32 v[234:235], v[234:235], v[238:239]
	v_pk_add_f32 v[236:237], v[236:237], v[240:241]
	v_cvt_pk_f32_fp8_e32 v[238:239], v90
	v_cvt_pk_f32_fp8_sdwa v[240:241], v90 src0_sel:WORD_1
	v_lshlrev_b32_e32 v244, 16, v109
	v_and_b32_e32 v245, 0xffff0000, v109
	v_pk_add_f32 v[234:235], v[234:235], v[238:239]
	v_pk_add_f32 v[236:237], v[236:237], v[240:241]
	v_cvt_pk_f32_fp8_e32 v[238:239], v91
	v_cvt_pk_f32_fp8_sdwa v[240:241], v91 src0_sel:WORD_1
	v_pk_mul_f32 v[242:243], v[242:243], s[8:9] op_sel_hi:[1,0]
	v_pk_mul_f32 v[244:245], v[244:245], s[8:9] op_sel_hi:[1,0]
	v_pk_add_f32 v[234:235], v[234:235], v[238:239]
	v_pk_add_f32 v[236:237], v[236:237], v[240:241]
	v_pk_fma_f32 v[136:137], v[136:137], v[234:235], v[242:243]
	v_pk_fma_f32 v[138:139], v[138:139], v[236:237], v[244:245]
	v_pk_add_f32 v[246:247], v[246:247], v[136:137]
	v_pk_add_f32 v[246:247], v[246:247], v[138:139]
	v_cvt_pk_f32_fp8_e32 v[234:235], v92
	v_cvt_pk_f32_fp8_sdwa v[236:237], v92 src0_sel:WORD_1
	v_cvt_pk_f32_fp8_e32 v[238:239], v93
	v_cvt_pk_f32_fp8_sdwa v[240:241], v93 src0_sel:WORD_1
	v_lshlrev_b32_e32 v242, 16, v110
	v_and_b32_e32 v243, 0xffff0000, v110
	v_pk_add_f32 v[234:235], v[234:235], v[238:239]
	v_pk_add_f32 v[236:237], v[236:237], v[240:241]
	v_cvt_pk_f32_fp8_e32 v[238:239], v94
	v_cvt_pk_f32_fp8_sdwa v[240:241], v94 src0_sel:WORD_1
	v_lshlrev_b32_e32 v244, 16, v111
	v_and_b32_e32 v245, 0xffff0000, v111
	v_pk_add_f32 v[234:235], v[234:235], v[238:239]
	v_pk_add_f32 v[236:237], v[236:237], v[240:241]
	v_cvt_pk_f32_fp8_e32 v[238:239], v95
	v_cvt_pk_f32_fp8_sdwa v[240:241], v95 src0_sel:WORD_1
	v_pk_mul_f32 v[242:243], v[242:243], s[8:9] op_sel_hi:[1,0]
	v_pk_mul_f32 v[244:245], v[244:245], s[8:9] op_sel_hi:[1,0]
	v_pk_add_f32 v[234:235], v[234:235], v[238:239]
	v_pk_add_f32 v[236:237], v[236:237], v[240:241]
	v_pk_fma_f32 v[140:141], v[140:141], v[234:235], v[242:243]
	v_pk_fma_f32 v[142:143], v[142:143], v[236:237], v[244:245]
	v_pk_add_f32 v[246:247], v[246:247], v[140:141]
	v_pk_add_f32 v[246:247], v[246:247], v[142:143]
	v_add_f32_e32 v246, v246, v247
	s_nop 1
	v_add_f32_dpp v246, v246, v246 quad_perm:[1,0,3,2] row_mask:0xf bank_mask:0xf
	s_nop 1
	v_add_f32_dpp v246, v246, v246 quad_perm:[2,3,0,1] row_mask:0xf bank_mask:0xf
	s_nop 1
	v_add_f32_dpp v246, v246, v246 row_half_mirror row_mask:0xf bank_mask:0xf
	s_nop 1
	v_add_f32_dpp v246, v246, v246 row_mirror row_mask:0xf bank_mask:0xf
	v_mov_b32_e32 v248, v246
	s_nop 1
	v_permlane16_swap_b32 v248, v246
	v_add_f32_e32 v246, v246, v248
	v_mov_b32_e32 v248, v246
	s_nop 1
	v_permlane32_swap_b32 v248, v246
	v_add_f32_e32 v246, v246, v248
	v_mul_f32_e32 v248, 0xba000000, v246
	v_pk_add_f32 v[112:113], v[112:113], v[248:249] op_sel_hi:[1,0]
	v_pk_add_f32 v[114:115], v[114:115], v[248:249] op_sel_hi:[1,0]
	v_pk_add_f32 v[116:117], v[116:117], v[248:249] op_sel_hi:[1,0]
	v_pk_add_f32 v[118:119], v[118:119], v[248:249] op_sel_hi:[1,0]
	v_pk_add_f32 v[120:121], v[120:121], v[248:249] op_sel_hi:[1,0]
	v_pk_add_f32 v[122:123], v[122:123], v[248:249] op_sel_hi:[1,0]
	v_pk_add_f32 v[124:125], v[124:125], v[248:249] op_sel_hi:[1,0]
	v_pk_add_f32 v[126:127], v[126:127], v[248:249] op_sel_hi:[1,0]
	v_pk_add_f32 v[128:129], v[128:129], v[248:249] op_sel_hi:[1,0]
	v_pk_add_f32 v[130:131], v[130:131], v[248:249] op_sel_hi:[1,0]
	v_pk_add_f32 v[132:133], v[132:133], v[248:249] op_sel_hi:[1,0]
	v_pk_add_f32 v[134:135], v[134:135], v[248:249] op_sel_hi:[1,0]
	v_pk_add_f32 v[136:137], v[136:137], v[248:249] op_sel_hi:[1,0]
	v_pk_add_f32 v[138:139], v[138:139], v[248:249] op_sel_hi:[1,0]
	v_pk_add_f32 v[140:141], v[140:141], v[248:249] op_sel_hi:[1,0]
	v_pk_add_f32 v[142:143], v[142:143], v[248:249] op_sel_hi:[1,0]
	v_pk_mul_f32 v[250:251], v[112:113], v[112:113]
	v_pk_fma_f32 v[250:251], v[114:115], v[114:115], v[250:251]
	v_pk_fma_f32 v[250:251], v[116:117], v[116:117], v[250:251]
	v_pk_fma_f32 v[250:251], v[118:119], v[118:119], v[250:251]
	v_pk_fma_f32 v[250:251], v[120:121], v[120:121], v[250:251]
	v_pk_fma_f32 v[250:251], v[122:123], v[122:123], v[250:251]
	v_pk_fma_f32 v[250:251], v[124:125], v[124:125], v[250:251]
	v_pk_fma_f32 v[250:251], v[126:127], v[126:127], v[250:251]
	v_pk_fma_f32 v[250:251], v[128:129], v[128:129], v[250:251]
	v_pk_fma_f32 v[250:251], v[130:131], v[130:131], v[250:251]
	v_pk_fma_f32 v[250:251], v[132:133], v[132:133], v[250:251]
	v_pk_fma_f32 v[250:251], v[134:135], v[134:135], v[250:251]
	v_pk_fma_f32 v[250:251], v[136:137], v[136:137], v[250:251]
	v_pk_fma_f32 v[250:251], v[138:139], v[138:139], v[250:251]
	v_pk_fma_f32 v[250:251], v[140:141], v[140:141], v[250:251]
	v_pk_fma_f32 v[250:251], v[142:143], v[142:143], v[250:251]
	v_add_f32_e32 v250, v250, v251
	s_nop 1
	v_add_f32_dpp v250, v250, v250 quad_perm:[1,0,3,2] row_mask:0xf bank_mask:0xf
	s_nop 1
	v_add_f32_dpp v250, v250, v250 quad_perm:[2,3,0,1] row_mask:0xf bank_mask:0xf
	s_nop 1
	v_add_f32_dpp v250, v250, v250 row_half_mirror row_mask:0xf bank_mask:0xf
	s_nop 1
	v_add_f32_dpp v250, v250, v250 row_mirror row_mask:0xf bank_mask:0xf
	v_mov_b32_e32 v248, v250
	s_nop 1
	v_permlane16_swap_b32 v248, v250
	v_add_f32_e32 v250, v250, v248
	v_mov_b32_e32 v248, v250
	s_nop 1
	v_permlane32_swap_b32 v248, v250
	v_add_f32_e32 v250, v250, v248
	v_mul_f32_e32 v234, 0x3a000000, v250
	v_add_f32_e32 v234, 0x3727c5ac, v234
	v_mul_f32_e32 v235, 0x4f800000, v234
	v_cmp_gt_f32_e32 vcc, s23, v234
	s_nop 1
	v_cndmask_b32_e32 v234, v234, v235, vcc
	v_sqrt_f32_e32 v235, v234
	s_nop 0
	v_add_u32_e32 v236, -1, v235
	v_add_u32_e32 v237, 1, v235
	v_fma_f32 v238, -v236, v235, v234
	v_fma_f32 v239, -v237, v235, v234
	v_cmp_ge_f32_e64 s[0:1], 0, v238
	s_nop 1
	v_cndmask_b32_e64 v235, v235, v236, s[0:1]
	v_cmp_lt_f32_e64 s[0:1], 0, v239
	s_nop 1
	v_cndmask_b32_e64 v235, v235, v237, s[0:1]
	v_mul_f32_e32 v236, 0x37800000, v235
	v_cndmask_b32_e32 v235, v235, v236, vcc
	v_cmp_class_f32_e64 vcc, v234, s22
	s_nop 1
	v_cndmask_b32_e32 v234, v235, v234, vcc
	v_div_scale_f32 v235, s[0:1], v234, v234, 1.0
	v_rcp_f32_e32 v237, v235
	v_div_scale_f32 v236, vcc, 1.0, v234, 1.0
	v_fma_f32 v238, -v235, v237, 1.0
	v_fmac_f32_e32 v237, v238, v237
	v_mul_f32_e32 v238, v236, v237
	v_fma_f32 v239, -v235, v238, v236
	v_fmac_f32_e32 v238, v239, v237
	v_fma_f32 v235, -v235, v238, v236
	v_div_fmas_f32 v235, v235, v237, v238
	v_div_fixup_f32 v234, v235, v234, 1.0
	v_pk_mul_f32 v[112:113], v[112:113], v[234:235] op_sel_hi:[1,0]
	v_pk_mul_f32 v[114:115], v[114:115], v[234:235] op_sel_hi:[1,0]
	v_pk_mul_f32 v[116:117], v[116:117], v[234:235] op_sel_hi:[1,0]
	v_pk_mul_f32 v[118:119], v[118:119], v[234:235] op_sel_hi:[1,0]
	v_pk_mul_f32 v[120:121], v[120:121], v[234:235] op_sel_hi:[1,0]
	v_pk_mul_f32 v[122:123], v[122:123], v[234:235] op_sel_hi:[1,0]
	v_pk_mul_f32 v[124:125], v[124:125], v[234:235] op_sel_hi:[1,0]
	v_pk_mul_f32 v[126:127], v[126:127], v[234:235] op_sel_hi:[1,0]
	v_pk_mul_f32 v[128:129], v[128:129], v[234:235] op_sel_hi:[1,0]
	v_pk_mul_f32 v[130:131], v[130:131], v[234:235] op_sel_hi:[1,0]
	v_pk_mul_f32 v[132:133], v[132:133], v[234:235] op_sel_hi:[1,0]
	v_pk_mul_f32 v[134:135], v[134:135], v[234:235] op_sel_hi:[1,0]
	v_pk_mul_f32 v[136:137], v[136:137], v[234:235] op_sel_hi:[1,0]
	v_pk_mul_f32 v[138:139], v[138:139], v[234:235] op_sel_hi:[1,0]
	v_pk_mul_f32 v[140:141], v[140:141], v[234:235] op_sel_hi:[1,0]
	v_pk_mul_f32 v[142:143], v[142:143], v[234:235] op_sel_hi:[1,0]
	v_pk_fma_f32 v[112:113], v[20:21], v[112:113], v[0:1]
	v_pk_fma_f32 v[114:115], v[22:23], v[114:115], v[2:3]
	v_pk_fma_f32 v[116:117], v[24:25], v[116:117], v[4:5]
	v_pk_fma_f32 v[118:119], v[26:27], v[118:119], v[6:7]
	v_pk_fma_f32 v[120:121], v[32:33], v[120:121], v[8:9]
	v_pk_fma_f32 v[122:123], v[34:35], v[122:123], v[10:11]
	v_pk_fma_f32 v[124:125], v[40:41], v[124:125], v[12:13]
	v_pk_fma_f32 v[126:127], v[42:43], v[126:127], v[14:15]
	v_pk_fma_f32 v[128:129], v[52:53], v[128:129], v[28:29]
	v_pk_fma_f32 v[130:131], v[54:55], v[130:131], v[30:31]
	v_pk_fma_f32 v[132:133], v[56:57], v[132:133], v[36:37]
	v_pk_fma_f32 v[134:135], v[58:59], v[134:135], v[38:39]
	v_pk_fma_f32 v[136:137], v[60:61], v[136:137], v[44:45]
	v_pk_fma_f32 v[138:139], v[62:63], v[138:139], v[46:47]
	v_pk_fma_f32 v[140:141], v[48:49], v[140:141], v[16:17]
	v_pk_fma_f32 v[142:143], v[50:51], v[142:143], v[18:19]
	s_lshl_b32 s0, s2, 13
	s_add_u32 s20, s26, s0
	s_addc_u32 s21, s27, 0
	global_store_dwordx4 v226, v[112:115], s[20:21] nt
	global_store_dwordx4 v226, v[116:119], s[20:21] offset:1024 nt
	global_store_dwordx4 v226, v[120:123], s[20:21] offset:2048 nt
	global_store_dwordx4 v226, v[124:127], s[20:21] offset:3072 nt
	global_store_dwordx4 v227, v[128:131], s[20:21] nt
	global_store_dwordx4 v227, v[132:135], s[20:21] offset:1024 nt
	global_store_dwordx4 v227, v[136:139], s[20:21] offset:2048 nt
	global_store_dwordx4 v227, v[140:143], s[20:21] offset:3072 nt
	s_mov_b32 s2, s3
	s_cmpk_lt_i32 s2, 0x2000
	s_cbranch_scc0 .LBB0_1225

.Lp9_nold_B:
	v_cvt_pk_f32_fp8_e32 v[234:235], v144
	v_cvt_pk_f32_fp8_sdwa v[236:237], v144 src0_sel:WORD_1
	v_cvt_pk_f32_fp8_e32 v[238:239], v145
	v_cvt_pk_f32_fp8_sdwa v[240:241], v145 src0_sel:WORD_1
	v_lshlrev_b32_e32 v242, 16, v176
	v_and_b32_e32 v243, 0xffff0000, v176
	v_pk_add_f32 v[234:235], v[234:235], v[238:239]
	v_pk_add_f32 v[236:237], v[236:237], v[240:241]
	v_cvt_pk_f32_fp8_e32 v[238:239], v146
	v_cvt_pk_f32_fp8_sdwa v[240:241], v146 src0_sel:WORD_1
	v_lshlrev_b32_e32 v244, 16, v177
	v_and_b32_e32 v245, 0xffff0000, v177
	v_pk_add_f32 v[234:235], v[234:235], v[238:239]
	v_pk_add_f32 v[236:237], v[236:237], v[240:241]
	v_cvt_pk_f32_fp8_e32 v[238:239], v147
	v_cvt_pk_f32_fp8_sdwa v[240:241], v147 src0_sel:WORD_1
	v_pk_mul_f32 v[242:243], v[242:243], s[8:9] op_sel_hi:[1,0]
	v_pk_mul_f32 v[244:245], v[244:245], s[8:9] op_sel_hi:[1,0]
	v_pk_add_f32 v[234:235], v[234:235], v[238:239]
	v_pk_add_f32 v[236:237], v[236:237], v[240:241]
	v_pk_fma_f32 v[192:193], v[192:193], v[234:235], v[242:243]
	v_pk_fma_f32 v[194:195], v[194:195], v[236:237], v[244:245]
	v_pk_add_f32 v[246:247], v[192:193], v[194:195]
	v_cvt_pk_f32_fp8_e32 v[234:235], v148
	v_cvt_pk_f32_fp8_sdwa v[236:237], v148 src0_sel:WORD_1
	v_cvt_pk_f32_fp8_e32 v[238:239], v149
	v_cvt_pk_f32_fp8_sdwa v[240:241], v149 src0_sel:WORD_1
	v_lshlrev_b32_e32 v242, 16, v178
	v_and_b32_e32 v243, 0xffff0000, v178
	v_pk_add_f32 v[234:235], v[234:235], v[238:239]
	v_pk_add_f32 v[236:237], v[236:237], v[240:241]
	v_cvt_pk_f32_fp8_e32 v[238:239], v150
	v_cvt_pk_f32_fp8_sdwa v[240:241], v150 src0_sel:WORD_1
	v_lshlrev_b32_e32 v244, 16, v179
	v_and_b32_e32 v245, 0xffff0000, v179
	v_pk_add_f32 v[234:235], v[234:235], v[238:239]
	v_pk_add_f32 v[236:237], v[236:237], v[240:241]
	v_cvt_pk_f32_fp8_e32 v[238:239], v151
	v_cvt_pk_f32_fp8_sdwa v[240:241], v151 src0_sel:WORD_1
	v_pk_mul_f32 v[242:243], v[242:243], s[8:9] op_sel_hi:[1,0]
	v_pk_mul_f32 v[244:245], v[244:245], s[8:9] op_sel_hi:[1,0]
	v_pk_add_f32 v[234:235], v[234:235], v[238:239]
	v_pk_add_f32 v[236:237], v[236:237], v[240:241]
	v_pk_fma_f32 v[196:197], v[196:197], v[234:235], v[242:243]
	v_pk_fma_f32 v[198:199], v[198:199], v[236:237], v[244:245]
	v_pk_add_f32 v[246:247], v[246:247], v[196:197]
	v_pk_add_f32 v[246:247], v[246:247], v[198:199]
	v_cvt_pk_f32_fp8_e32 v[234:235], v152
	v_cvt_pk_f32_fp8_sdwa v[236:237], v152 src0_sel:WORD_1
	v_cvt_pk_f32_fp8_e32 v[238:239], v153
	v_cvt_pk_f32_fp8_sdwa v[240:241], v153 src0_sel:WORD_1
	v_lshlrev_b32_e32 v242, 16, v180
	v_and_b32_e32 v243, 0xffff0000, v180
	v_pk_add_f32 v[234:235], v[234:235], v[238:239]
	v_pk_add_f32 v[236:237], v[236:237], v[240:241]
	v_cvt_pk_f32_fp8_e32 v[238:239], v154
	v_cvt_pk_f32_fp8_sdwa v[240:241], v154 src0_sel:WORD_1
	v_lshlrev_b32_e32 v244, 16, v181
	v_and_b32_e32 v245, 0xffff0000, v181
	v_pk_add_f32 v[234:235], v[234:235], v[238:239]
	v_pk_add_f32 v[236:237], v[236:237], v[240:241]
	v_cvt_pk_f32_fp8_e32 v[238:239], v155
	v_cvt_pk_f32_fp8_sdwa v[240:241], v155 src0_sel:WORD_1
	v_pk_mul_f32 v[242:243], v[242:243], s[8:9] op_sel_hi:[1,0]
	v_pk_mul_f32 v[244:245], v[244:245], s[8:9] op_sel_hi:[1,0]
	v_pk_add_f32 v[234:235], v[234:235], v[238:239]
	v_pk_add_f32 v[236:237], v[236:237], v[240:241]
	v_pk_fma_f32 v[200:201], v[200:201], v[234:235], v[242:243]
	v_pk_fma_f32 v[202:203], v[202:203], v[236:237], v[244:245]
	v_pk_add_f32 v[246:247], v[246:247], v[200:201]
	v_pk_add_f32 v[246:247], v[246:247], v[202:203]
	v_cvt_pk_f32_fp8_e32 v[234:235], v156
	v_cvt_pk_f32_fp8_sdwa v[236:237], v156 src0_sel:WORD_1
	v_cvt_pk_f32_fp8_e32 v[238:239], v157
	v_cvt_pk_f32_fp8_sdwa v[240:241], v157 src0_sel:WORD_1
	v_lshlrev_b32_e32 v242, 16, v182
	v_and_b32_e32 v243, 0xffff0000, v182
	v_pk_add_f32 v[234:235], v[234:235], v[238:239]
	v_pk_add_f32 v[236:237], v[236:237], v[240:241]
	v_cvt_pk_f32_fp8_e32 v[238:239], v158
	v_cvt_pk_f32_fp8_sdwa v[240:241], v158 src0_sel:WORD_1
	v_lshlrev_b32_e32 v244, 16, v183
	v_and_b32_e32 v245, 0xffff0000, v183
	v_pk_add_f32 v[234:235], v[234:235], v[238:239]
	v_pk_add_f32 v[236:237], v[236:237], v[240:241]
	v_cvt_pk_f32_fp8_e32 v[238:239], v159
	v_cvt_pk_f32_fp8_sdwa v[240:241], v159 src0_sel:WORD_1
	v_pk_mul_f32 v[242:243], v[242:243], s[8:9] op_sel_hi:[1,0]
	v_pk_mul_f32 v[244:245], v[244:245], s[8:9] op_sel_hi:[1,0]
	v_pk_add_f32 v[234:235], v[234:235], v[238:239]
	v_pk_add_f32 v[236:237], v[236:237], v[240:241]
	v_pk_fma_f32 v[204:205], v[204:205], v[234:235], v[242:243]
	v_pk_fma_f32 v[206:207], v[206:207], v[236:237], v[244:245]
	v_pk_add_f32 v[246:247], v[246:247], v[204:205]
	v_pk_add_f32 v[246:247], v[246:247], v[206:207]
	v_cvt_pk_f32_fp8_e32 v[234:235], v160
	v_cvt_pk_f32_fp8_sdwa v[236:237], v160 src0_sel:WORD_1
	v_cvt_pk_f32_fp8_e32 v[238:239], v161
	v_cvt_pk_f32_fp8_sdwa v[240:241], v161 src0_sel:WORD_1
	v_lshlrev_b32_e32 v242, 16, v184
	v_and_b32_e32 v243, 0xffff0000, v184
	v_pk_add_f32 v[234:235], v[234:235], v[238:239]
	v_pk_add_f32 v[236:237], v[236:237], v[240:241]
	v_cvt_pk_f32_fp8_e32 v[238:239], v162
	v_cvt_pk_f32_fp8_sdwa v[240:241], v162 src0_sel:WORD_1
	v_lshlrev_b32_e32 v244, 16, v185
	v_and_b32_e32 v245, 0xffff0000, v185
	v_pk_add_f32 v[234:235], v[234:235], v[238:239]
	v_pk_add_f32 v[236:237], v[236:237], v[240:241]
	v_cvt_pk_f32_fp8_e32 v[238:239], v163
	v_cvt_pk_f32_fp8_sdwa v[240:241], v163 src0_sel:WORD_1
	v_pk_mul_f32 v[242:243], v[242:243], s[8:9] op_sel_hi:[1,0]
	v_pk_mul_f32 v[244:245], v[244:245], s[8:9] op_sel_hi:[1,0]
	v_pk_add_f32 v[234:235], v[234:235], v[238:239]
	v_pk_add_f32 v[236:237], v[236:237], v[240:241]
	v_pk_fma_f32 v[208:209], v[208:209], v[234:235], v[242:243]
	v_pk_fma_f32 v[210:211], v[210:211], v[236:237], v[244:245]
	v_pk_add_f32 v[246:247], v[246:247], v[208:209]
	v_pk_add_f32 v[246:247], v[246:247], v[210:211]
	v_cvt_pk_f32_fp8_e32 v[234:235], v164
	v_cvt_pk_f32_fp8_sdwa v[236:237], v164 src0_sel:WORD_1
	v_cvt_pk_f32_fp8_e32 v[238:239], v165
	v_cvt_pk_f32_fp8_sdwa v[240:241], v165 src0_sel:WORD_1
	v_lshlrev_b32_e32 v242, 16, v186
	v_and_b32_e32 v243, 0xffff0000, v186
	v_pk_add_f32 v[234:235], v[234:235], v[238:239]
	v_pk_add_f32 v[236:237], v[236:237], v[240:241]
	v_cvt_pk_f32_fp8_e32 v[238:239], v166
	v_cvt_pk_f32_fp8_sdwa v[240:241], v166 src0_sel:WORD_1
	v_lshlrev_b32_e32 v244, 16, v187
	v_and_b32_e32 v245, 0xffff0000, v187
	v_pk_add_f32 v[234:235], v[234:235], v[238:239]
	v_pk_add_f32 v[236:237], v[236:237], v[240:241]
	v_cvt_pk_f32_fp8_e32 v[238:239], v167
	v_cvt_pk_f32_fp8_sdwa v[240:241], v167 src0_sel:WORD_1
	v_pk_mul_f32 v[242:243], v[242:243], s[8:9] op_sel_hi:[1,0]
	v_pk_mul_f32 v[244:245], v[244:245], s[8:9] op_sel_hi:[1,0]
	v_pk_add_f32 v[234:235], v[234:235], v[238:239]
	v_pk_add_f32 v[236:237], v[236:237], v[240:241]
	v_pk_fma_f32 v[212:213], v[212:213], v[234:235], v[242:243]
	v_pk_fma_f32 v[214:215], v[214:215], v[236:237], v[244:245]
	v_pk_add_f32 v[246:247], v[246:247], v[212:213]
	v_pk_add_f32 v[246:247], v[246:247], v[214:215]
	v_cvt_pk_f32_fp8_e32 v[234:235], v168
	v_cvt_pk_f32_fp8_sdwa v[236:237], v168 src0_sel:WORD_1
	v_cvt_pk_f32_fp8_e32 v[238:239], v169
	v_cvt_pk_f32_fp8_sdwa v[240:241], v169 src0_sel:WORD_1
	v_lshlrev_b32_e32 v242, 16, v188
	v_and_b32_e32 v243, 0xffff0000, v188
	v_pk_add_f32 v[234:235], v[234:235], v[238:239]
	v_pk_add_f32 v[236:237], v[236:237], v[240:241]
	v_cvt_pk_f32_fp8_e32 v[238:239], v170
	v_cvt_pk_f32_fp8_sdwa v[240:241], v170 src0_sel:WORD_1
	v_lshlrev_b32_e32 v244, 16, v189
	v_and_b32_e32 v245, 0xffff0000, v189
	v_pk_add_f32 v[234:235], v[234:235], v[238:239]
	v_pk_add_f32 v[236:237], v[236:237], v[240:241]
	v_cvt_pk_f32_fp8_e32 v[238:239], v171
	v_cvt_pk_f32_fp8_sdwa v[240:241], v171 src0_sel:WORD_1
	v_pk_mul_f32 v[242:243], v[242:243], s[8:9] op_sel_hi:[1,0]
	v_pk_mul_f32 v[244:245], v[244:245], s[8:9] op_sel_hi:[1,0]
	v_pk_add_f32 v[234:235], v[234:235], v[238:239]
	v_pk_add_f32 v[236:237], v[236:237], v[240:241]
	v_pk_fma_f32 v[216:217], v[216:217], v[234:235], v[242:243]
	v_pk_fma_f32 v[218:219], v[218:219], v[236:237], v[244:245]
	v_pk_add_f32 v[246:247], v[246:247], v[216:217]
	v_pk_add_f32 v[246:247], v[246:247], v[218:219]
	v_cvt_pk_f32_fp8_e32 v[234:235], v172
	v_cvt_pk_f32_fp8_sdwa v[236:237], v172 src0_sel:WORD_1
	v_cvt_pk_f32_fp8_e32 v[238:239], v173
	v_cvt_pk_f32_fp8_sdwa v[240:241], v173 src0_sel:WORD_1
	v_lshlrev_b32_e32 v242, 16, v190
	v_and_b32_e32 v243, 0xffff0000, v190
	v_pk_add_f32 v[234:235], v[234:235], v[238:239]
	v_pk_add_f32 v[236:237], v[236:237], v[240:241]
	v_cvt_pk_f32_fp8_e32 v[238:239], v174
	v_cvt_pk_f32_fp8_sdwa v[240:241], v174 src0_sel:WORD_1
	v_lshlrev_b32_e32 v244, 16, v191
	v_and_b32_e32 v245, 0xffff0000, v191
	v_pk_add_f32 v[234:235], v[234:235], v[238:239]
	v_pk_add_f32 v[236:237], v[236:237], v[240:241]
	v_cvt_pk_f32_fp8_e32 v[238:239], v175
	v_cvt_pk_f32_fp8_sdwa v[240:241], v175 src0_sel:WORD_1
	v_pk_mul_f32 v[242:243], v[242:243], s[8:9] op_sel_hi:[1,0]
	v_pk_mul_f32 v[244:245], v[244:245], s[8:9] op_sel_hi:[1,0]
	v_pk_add_f32 v[234:235], v[234:235], v[238:239]
	v_pk_add_f32 v[236:237], v[236:237], v[240:241]
	v_pk_fma_f32 v[220:221], v[220:221], v[234:235], v[242:243]
	v_pk_fma_f32 v[222:223], v[222:223], v[236:237], v[244:245]
	v_pk_add_f32 v[246:247], v[246:247], v[220:221]
	v_pk_add_f32 v[246:247], v[246:247], v[222:223]
	v_add_f32_e32 v246, v246, v247
	s_nop 1
	v_add_f32_dpp v246, v246, v246 quad_perm:[1,0,3,2] row_mask:0xf bank_mask:0xf
	s_nop 1
	v_add_f32_dpp v246, v246, v246 quad_perm:[2,3,0,1] row_mask:0xf bank_mask:0xf
	s_nop 1
	v_add_f32_dpp v246, v246, v246 row_half_mirror row_mask:0xf bank_mask:0xf
	s_nop 1
	v_add_f32_dpp v246, v246, v246 row_mirror row_mask:0xf bank_mask:0xf
	v_mov_b32_e32 v248, v246
	s_nop 1
	v_permlane16_swap_b32 v248, v246
	v_add_f32_e32 v246, v246, v248
	v_mov_b32_e32 v248, v246
	s_nop 1
	v_permlane32_swap_b32 v248, v246
	v_add_f32_e32 v246, v246, v248
	v_mul_f32_e32 v248, 0xba000000, v246
	v_pk_add_f32 v[192:193], v[192:193], v[248:249] op_sel_hi:[1,0]
	v_pk_add_f32 v[194:195], v[194:195], v[248:249] op_sel_hi:[1,0]
	v_pk_add_f32 v[196:197], v[196:197], v[248:249] op_sel_hi:[1,0]
	v_pk_add_f32 v[198:199], v[198:199], v[248:249] op_sel_hi:[1,0]
	v_pk_add_f32 v[200:201], v[200:201], v[248:249] op_sel_hi:[1,0]
	v_pk_add_f32 v[202:203], v[202:203], v[248:249] op_sel_hi:[1,0]
	v_pk_add_f32 v[204:205], v[204:205], v[248:249] op_sel_hi:[1,0]
	v_pk_add_f32 v[206:207], v[206:207], v[248:249] op_sel_hi:[1,0]
	v_pk_add_f32 v[208:209], v[208:209], v[248:249] op_sel_hi:[1,0]
	v_pk_add_f32 v[210:211], v[210:211], v[248:249] op_sel_hi:[1,0]
	v_pk_add_f32 v[212:213], v[212:213], v[248:249] op_sel_hi:[1,0]
	v_pk_add_f32 v[214:215], v[214:215], v[248:249] op_sel_hi:[1,0]
	v_pk_add_f32 v[216:217], v[216:217], v[248:249] op_sel_hi:[1,0]
	v_pk_add_f32 v[218:219], v[218:219], v[248:249] op_sel_hi:[1,0]
	v_pk_add_f32 v[220:221], v[220:221], v[248:249] op_sel_hi:[1,0]
	v_pk_add_f32 v[222:223], v[222:223], v[248:249] op_sel_hi:[1,0]
	v_pk_mul_f32 v[250:251], v[192:193], v[192:193]
	v_pk_fma_f32 v[250:251], v[194:195], v[194:195], v[250:251]
	v_pk_fma_f32 v[250:251], v[196:197], v[196:197], v[250:251]
	v_pk_fma_f32 v[250:251], v[198:199], v[198:199], v[250:251]
	v_pk_fma_f32 v[250:251], v[200:201], v[200:201], v[250:251]
	v_pk_fma_f32 v[250:251], v[202:203], v[202:203], v[250:251]
	v_pk_fma_f32 v[250:251], v[204:205], v[204:205], v[250:251]
	v_pk_fma_f32 v[250:251], v[206:207], v[206:207], v[250:251]
	v_pk_fma_f32 v[250:251], v[208:209], v[208:209], v[250:251]
	v_pk_fma_f32 v[250:251], v[210:211], v[210:211], v[250:251]
	v_pk_fma_f32 v[250:251], v[212:213], v[212:213], v[250:251]
	v_pk_fma_f32 v[250:251], v[214:215], v[214:215], v[250:251]
	v_pk_fma_f32 v[250:251], v[216:217], v[216:217], v[250:251]
	v_pk_fma_f32 v[250:251], v[218:219], v[218:219], v[250:251]
	v_pk_fma_f32 v[250:251], v[220:221], v[220:221], v[250:251]
	v_pk_fma_f32 v[250:251], v[222:223], v[222:223], v[250:251]
	v_add_f32_e32 v250, v250, v251
	s_nop 1
	v_add_f32_dpp v250, v250, v250 quad_perm:[1,0,3,2] row_mask:0xf bank_mask:0xf
	s_nop 1
	v_add_f32_dpp v250, v250, v250 quad_perm:[2,3,0,1] row_mask:0xf bank_mask:0xf
	s_nop 1
	v_add_f32_dpp v250, v250, v250 row_half_mirror row_mask:0xf bank_mask:0xf
	s_nop 1
	v_add_f32_dpp v250, v250, v250 row_mirror row_mask:0xf bank_mask:0xf
	v_mov_b32_e32 v248, v250
	s_nop 1
	v_permlane16_swap_b32 v248, v250
	v_add_f32_e32 v250, v250, v248
	v_mov_b32_e32 v248, v250
	s_nop 1
	v_permlane32_swap_b32 v248, v250
	v_add_f32_e32 v250, v250, v248
	v_mul_f32_e32 v234, 0x3a000000, v250
	v_add_f32_e32 v234, 0x3727c5ac, v234
	v_mul_f32_e32 v235, 0x4f800000, v234
	v_cmp_gt_f32_e32 vcc, s23, v234
	s_nop 1
	v_cndmask_b32_e32 v234, v234, v235, vcc
	v_sqrt_f32_e32 v235, v234
	s_nop 0
	v_add_u32_e32 v236, -1, v235
	v_add_u32_e32 v237, 1, v235
	v_fma_f32 v238, -v236, v235, v234
	v_fma_f32 v239, -v237, v235, v234
	v_cmp_ge_f32_e64 s[0:1], 0, v238
	s_nop 1
	v_cndmask_b32_e64 v235, v235, v236, s[0:1]
	v_cmp_lt_f32_e64 s[0:1], 0, v239
	s_nop 1
	v_cndmask_b32_e64 v235, v235, v237, s[0:1]
	v_mul_f32_e32 v236, 0x37800000, v235
	v_cndmask_b32_e32 v235, v235, v236, vcc
	v_cmp_class_f32_e64 vcc, v234, s22
	s_nop 1
	v_cndmask_b32_e32 v234, v235, v234, vcc
	v_div_scale_f32 v235, s[0:1], v234, v234, 1.0
	v_rcp_f32_e32 v237, v235
	v_div_scale_f32 v236, vcc, 1.0, v234, 1.0
	v_fma_f32 v238, -v235, v237, 1.0
	v_fmac_f32_e32 v237, v238, v237
	v_mul_f32_e32 v238, v236, v237
	v_fma_f32 v239, -v235, v238, v236
	v_fmac_f32_e32 v238, v239, v237
	v_fma_f32 v235, -v235, v238, v236
	v_div_fmas_f32 v235, v235, v237, v238
	v_div_fixup_f32 v234, v235, v234, 1.0
	v_pk_mul_f32 v[192:193], v[192:193], v[234:235] op_sel_hi:[1,0]
	v_pk_mul_f32 v[194:195], v[194:195], v[234:235] op_sel_hi:[1,0]
	v_pk_mul_f32 v[196:197], v[196:197], v[234:235] op_sel_hi:[1,0]
	v_pk_mul_f32 v[198:199], v[198:199], v[234:235] op_sel_hi:[1,0]
	v_pk_mul_f32 v[200:201], v[200:201], v[234:235] op_sel_hi:[1,0]
	v_pk_mul_f32 v[202:203], v[202:203], v[234:235] op_sel_hi:[1,0]
	v_pk_mul_f32 v[204:205], v[204:205], v[234:235] op_sel_hi:[1,0]
	v_pk_mul_f32 v[206:207], v[206:207], v[234:235] op_sel_hi:[1,0]
	v_pk_mul_f32 v[208:209], v[208:209], v[234:235] op_sel_hi:[1,0]
	v_pk_mul_f32 v[210:211], v[210:211], v[234:235] op_sel_hi:[1,0]
	v_pk_mul_f32 v[212:213], v[212:213], v[234:235] op_sel_hi:[1,0]
	v_pk_mul_f32 v[214:215], v[214:215], v[234:235] op_sel_hi:[1,0]
	v_pk_mul_f32 v[216:217], v[216:217], v[234:235] op_sel_hi:[1,0]
	v_pk_mul_f32 v[218:219], v[218:219], v[234:235] op_sel_hi:[1,0]
	v_pk_mul_f32 v[220:221], v[220:221], v[234:235] op_sel_hi:[1,0]
	v_pk_mul_f32 v[222:223], v[222:223], v[234:235] op_sel_hi:[1,0]
	v_pk_fma_f32 v[192:193], v[20:21], v[192:193], v[0:1]
	v_pk_fma_f32 v[194:195], v[22:23], v[194:195], v[2:3]
	v_pk_fma_f32 v[196:197], v[24:25], v[196:197], v[4:5]
	v_pk_fma_f32 v[198:199], v[26:27], v[198:199], v[6:7]
	v_pk_fma_f32 v[200:201], v[32:33], v[200:201], v[8:9]
	v_pk_fma_f32 v[202:203], v[34:35], v[202:203], v[10:11]
	v_pk_fma_f32 v[204:205], v[40:41], v[204:205], v[12:13]
	v_pk_fma_f32 v[206:207], v[42:43], v[206:207], v[14:15]
	v_pk_fma_f32 v[208:209], v[52:53], v[208:209], v[28:29]
	v_pk_fma_f32 v[210:211], v[54:55], v[210:211], v[30:31]
	v_pk_fma_f32 v[212:213], v[56:57], v[212:213], v[36:37]
	v_pk_fma_f32 v[214:215], v[58:59], v[214:215], v[38:39]
	v_pk_fma_f32 v[216:217], v[60:61], v[216:217], v[44:45]
	v_pk_fma_f32 v[218:219], v[62:63], v[218:219], v[46:47]
	v_pk_fma_f32 v[220:221], v[48:49], v[220:221], v[16:17]
	v_pk_fma_f32 v[222:223], v[50:51], v[222:223], v[18:19]
	s_lshl_b32 s0, s2, 13
	s_add_u32 s20, s26, s0
	s_addc_u32 s21, s27, 0
	global_store_dwordx4 v226, v[192:195], s[20:21] nt
	global_store_dwordx4 v226, v[196:199], s[20:21] offset:1024 nt
	global_store_dwordx4 v226, v[200:203], s[20:21] offset:2048 nt
	global_store_dwordx4 v226, v[204:207], s[20:21] offset:3072 nt
	global_store_dwordx4 v227, v[208:211], s[20:21] nt
	global_store_dwordx4 v227, v[212:215], s[20:21] offset:1024 nt
	global_store_dwordx4 v227, v[216:219], s[20:21] offset:2048 nt
	global_store_dwordx4 v227, v[220:223], s[20:21] offset:3072 nt
	s_mov_b32 s2, s3
	s_cmpk_lt_i32 s2, 0x2000
	s_cbranch_scc1 .Lp9_top_A
